# k_prep compose staging: 2-trip load/drain/LDS-write loop unrolled with the second trip's 16 loads in flight before the first trip's waits (renamed registers, accum_offset 80)
# baseline (speedup 1.0000x reference)
.LBB0_126:
	global_load_dword v6, v[4:5], off
	global_load_dword v20, v[4:5], off offset:1024
	global_load_dword v21, v[4:5], off offset:2048
	global_load_dword v22, v[4:5], off offset:3072
	v_add_co_u32_e32 v24, vcc, 0x1000, v4
	s_nop 1
	v_addc_co_u32_e32 v25, vcc, 0, v5, vcc
	v_cmp_gt_u32_e32 vcc, 0x80, v0
	s_nop 1
	s_and_saveexec_b64 s[0:1], vcc
	global_load_dword v23, v[24:25], off
	s_or_b64 exec, exec, s[0:1]
	s_waitcnt vmcnt(0) lgkmcnt(0)
	ds_write_b32 v3, v6
	ds_write_b32 v3, v20 offset:1024
	ds_write_b32 v3, v21 offset:2048
	ds_write_b32 v3, v22 offset:3072
	s_and_saveexec_b64 s[0:1], vcc
	ds_write_b32 v3, v23 offset:4096
	s_or_b64 exec, exec, s[0:1]
	s_mov_b64 s[0:1], 0
	s_or_b64 exec, exec, s[0:1]
	v_or_b32_e32 v1, 0x100, v0
	v_mov_b32_e32 v8, 16
	s_mov_b64 s[0:1], 0
	v_mov_b32_e32 v7, 0
	v_mov_b32_e32 v3, v2
	v_mov_b64_e32 v[4:5], v[0:1]
	v_mov_b32_e32 v6, v4
	v_lshl_add_u64 v[24:25], v[6:7], 2, s[18:19]
	v_mov_b32_e32 v6, v5
	v_add_u32_e32 v10, 0x200, v5
	v_mov_b32_e32 v11, v7
	v_lshl_add_u64 v[26:27], v[6:7], 2, s[18:19]
	v_add_u32_e32 v6, 0x200, v4
	v_lshl_add_u64 v[10:11], v[10:11], 2, s[18:19]
	global_load_dword v1, v[24:25], off
	v_lshl_add_u64 v[24:25], v[6:7], 2, s[18:19]
	v_add_u32_e32 v6, 0x400, v4
	global_load_dword v9, v[26:27], off
	global_load_dword v28, v[24:25], off
	global_load_dword v29, v[10:11], off
	v_lshl_add_u64 v[10:11], v[6:7], 2, s[18:19]
	v_add_u32_e32 v6, 0x600, v4
	v_add_u32_e32 v12, 0x400, v5
	v_mov_b32_e32 v13, v7
	v_add_u32_e32 v14, 0x600, v5
	v_mov_b32_e32 v15, v7
	v_lshl_add_u64 v[24:25], v[6:7], 2, s[18:19]
	v_add_u32_e32 v6, 0x800, v4
	v_lshl_add_u64 v[12:13], v[12:13], 2, s[18:19]
	v_lshl_add_u64 v[14:15], v[14:15], 2, s[18:19]
	global_load_dword v26, v[10:11], off
	global_load_dword v27, v[12:13], off
	global_load_dword v30, v[24:25], off
	global_load_dword v31, v[14:15], off
	v_lshl_add_u64 v[10:11], v[6:7], 2, s[18:19]
	v_add_u32_e32 v6, 0xa00, v4
	v_add_u32_e32 v16, 0x800, v5
	v_mov_b32_e32 v17, v7
	v_add_u32_e32 v18, 0xa00, v5
	v_mov_b32_e32 v19, v7
	v_lshl_add_u64 v[12:13], v[6:7], 2, s[18:19]
	v_add_u32_e32 v6, 0xc00, v4
	v_add_u32_e32 v20, 0xc00, v5
	v_mov_b32_e32 v21, v7
	v_add_u32_e32 v22, 0xe00, v5
	v_mov_b32_e32 v23, v7
	v_lshl_add_u64 v[16:17], v[16:17], 2, s[18:19]
	v_lshl_add_u64 v[18:19], v[18:19], 2, s[18:19]
	global_load_dword v14, v[10:11], off
	global_load_dword v15, v[16:17], off
	global_load_dword v24, v[12:13], off
	global_load_dword v25, v[18:19], off
	v_lshl_add_u64 v[10:11], v[6:7], 2, s[18:19]
	v_add_u32_e32 v6, 0xe00, v4
	v_lshl_add_u64 v[20:21], v[20:21], 2, s[18:19]
	v_lshl_add_u64 v[22:23], v[22:23], 2, s[18:19]
	v_lshl_add_u64 v[12:13], v[6:7], 2, s[18:19]
	global_load_dword v6, v[10:11], off
	global_load_dword v16, v[20:21], off
	global_load_dword v17, v[12:13], off
	global_load_dword v18, v[22:23], off
	v_add_u32_e32 v5, 0x1000, v5
	v_add_u32_e32 v4, 0x1000, v4
	v_mov_b32_e32 v47, 0
	v_mov_b32_e32 v46, v4
	v_lshl_add_u64 v[64:65], v[46:47], 2, s[18:19]
	v_mov_b32_e32 v46, v5
	v_add_u32_e32 v50, 0x200, v5
	v_mov_b32_e32 v51, v47
	v_lshl_add_u64 v[66:67], v[46:47], 2, s[18:19]
	v_add_u32_e32 v46, 0x200, v4
	v_lshl_add_u64 v[50:51], v[50:51], 2, s[18:19]
	global_load_dword v41, v[64:65], off
	v_lshl_add_u64 v[64:65], v[46:47], 2, s[18:19]
	v_add_u32_e32 v46, 0x400, v4
	global_load_dword v49, v[66:67], off
	global_load_dword v68, v[64:65], off
	global_load_dword v69, v[50:51], off
	v_lshl_add_u64 v[50:51], v[46:47], 2, s[18:19]
	v_add_u32_e32 v46, 0x600, v4
	v_add_u32_e32 v52, 0x400, v5
	v_mov_b32_e32 v53, v47
	v_add_u32_e32 v54, 0x600, v5
	v_mov_b32_e32 v55, v47
	v_lshl_add_u64 v[64:65], v[46:47], 2, s[18:19]
	v_add_u32_e32 v46, 0x800, v4
	v_lshl_add_u64 v[52:53], v[52:53], 2, s[18:19]
	v_lshl_add_u64 v[54:55], v[54:55], 2, s[18:19]
	global_load_dword v66, v[50:51], off
	global_load_dword v67, v[52:53], off
	global_load_dword v70, v[64:65], off
	global_load_dword v71, v[54:55], off
	v_lshl_add_u64 v[50:51], v[46:47], 2, s[18:19]
	v_add_u32_e32 v46, 0xa00, v4
	v_add_u32_e32 v56, 0x800, v5
	v_mov_b32_e32 v57, v47
	v_add_u32_e32 v58, 0xa00, v5
	v_mov_b32_e32 v59, v47
	v_lshl_add_u64 v[52:53], v[46:47], 2, s[18:19]
	v_add_u32_e32 v46, 0xc00, v4
	v_add_u32_e32 v60, 0xc00, v5
	v_mov_b32_e32 v61, v47
	v_add_u32_e32 v62, 0xe00, v5
	v_mov_b32_e32 v63, v47
	v_lshl_add_u64 v[56:57], v[56:57], 2, s[18:19]
	v_lshl_add_u64 v[58:59], v[58:59], 2, s[18:19]
	global_load_dword v54, v[50:51], off
	global_load_dword v55, v[56:57], off
	global_load_dword v64, v[52:53], off
	global_load_dword v65, v[58:59], off
	v_lshl_add_u64 v[50:51], v[46:47], 2, s[18:19]
	v_add_u32_e32 v46, 0xe00, v4
	v_lshl_add_u64 v[60:61], v[60:61], 2, s[18:19]
	v_lshl_add_u64 v[62:63], v[62:63], 2, s[18:19]
	v_lshl_add_u64 v[52:53], v[46:47], 2, s[18:19]
	global_load_dword v46, v[50:51], off
	global_load_dword v56, v[60:61], off
	global_load_dword v57, v[52:53], off
	global_load_dword v58, v[62:63], off
	s_waitcnt vmcnt(30)
	ds_write2st64_b32 v3, v1, v9 offset1:4
	s_waitcnt vmcnt(28)
	ds_write2st64_b32 v3, v28, v29 offset0:8 offset1:12
	s_waitcnt vmcnt(26)
	ds_write2st64_b32 v3, v26, v27 offset0:16 offset1:20
	s_waitcnt vmcnt(24)
	ds_write2st64_b32 v3, v30, v31 offset0:24 offset1:28
	s_waitcnt vmcnt(22)
	ds_write2st64_b32 v3, v14, v15 offset0:32 offset1:36
	s_waitcnt vmcnt(20)
	ds_write2st64_b32 v3, v24, v25 offset0:40 offset1:44
	s_waitcnt vmcnt(18)
	ds_write2st64_b32 v3, v6, v16 offset0:48 offset1:52
	s_waitcnt vmcnt(16)
	ds_write2st64_b32 v3, v17, v18 offset0:56 offset1:60
	v_add_u32_e32 v3, 0x4000, v3
	s_waitcnt vmcnt(14)
	ds_write2st64_b32 v3, v41, v49 offset1:4
	s_waitcnt vmcnt(12)
	ds_write2st64_b32 v3, v68, v69 offset0:8 offset1:12
	s_waitcnt vmcnt(10)
	ds_write2st64_b32 v3, v66, v67 offset0:16 offset1:20
	s_waitcnt vmcnt(8)
	ds_write2st64_b32 v3, v70, v71 offset0:24 offset1:28
	s_waitcnt vmcnt(6)
	ds_write2st64_b32 v3, v54, v55 offset0:32 offset1:36
	s_waitcnt vmcnt(4)
	ds_write2st64_b32 v3, v64, v65 offset0:40 offset1:44
	s_waitcnt vmcnt(2)
	ds_write2st64_b32 v3, v46, v56 offset0:48 offset1:52
	s_waitcnt vmcnt(0)
	ds_write2st64_b32 v3, v57, v58 offset0:56 offset1:60
	v_add_u32_e32 v3, 0x4000, v3
	v_add_u32_e32 v5, 0x1000, v5
	v_add_u32_e32 v4, 0x1000, v4
	v_mov_b32_e32 v8, 0
	s_or_b64 exec, exec, s[0:1]
	v_mov_b32_e32 v1, 0
	v_cmp_ne_u32_e64 s[4:5], 0, 0
	s_and_saveexec_b64 s[0:1], s[4:5]
	s_cbranch_execz .LBB0_132
	s_mov_b64 s[4:5], 0
	v_mov_b32_e32 v7, 0

	.amdhsa_kernel _Z6k_prep8PrepArgsPKfS1_S1_S1_PDv8_DF16_PfS1_S4_
		.amdhsa_group_segment_fixed_size 37412
		.amdhsa_private_segment_fixed_size 0
		.amdhsa_kernarg_size 264
		.amdhsa_user_sgpr_count 2
		.amdhsa_user_sgpr_dispatch_ptr 0
		.amdhsa_user_sgpr_queue_ptr 0
		.amdhsa_user_sgpr_kernarg_segment_ptr 1
		.amdhsa_user_sgpr_dispatch_id 0
		.amdhsa_user_sgpr_kernarg_preload_length 0
		.amdhsa_user_sgpr_kernarg_preload_offset 0
		.amdhsa_user_sgpr_private_segment_size 0
		.amdhsa_uses_dynamic_stack 0
		.amdhsa_enable_private_segment 0
		.amdhsa_system_sgpr_workgroup_id_x 1
		.amdhsa_system_sgpr_workgroup_id_y 0
		.amdhsa_system_sgpr_workgroup_id_z 0
		.amdhsa_system_sgpr_workgroup_info 0
		.amdhsa_system_vgpr_workitem_id 0
		.amdhsa_next_free_vgpr 97
		.amdhsa_next_free_sgpr 96
		.amdhsa_accum_offset 80
		.amdhsa_reserve_vcc 1
		.amdhsa_float_round_mode_32 0
		.amdhsa_float_round_mode_16_64 0
		.amdhsa_float_denorm_mode_32 3
		.amdhsa_float_denorm_mode_16_64 3
		.amdhsa_dx10_clamp 1
		.amdhsa_ieee_mode 1
		.amdhsa_fp16_overflow 0
		.amdhsa_tg_split 0
		.amdhsa_exception_fp_ieee_invalid_op 0
		.amdhsa_exception_fp_denorm_src 0
		.amdhsa_exception_fp_ieee_div_zero 0
		.amdhsa_exception_fp_ieee_overflow 0
		.amdhsa_exception_fp_ieee_underflow 0
		.amdhsa_exception_fp_ieee_inexact 0
		.amdhsa_exception_int_div_zero 0
	.end_amdhsa_kernel

amdhsa.kernels:
  - .agpr_count:     0
    .args:
      - .offset:         0
        .size:           200
        .value_kind:     by_value
      - .actual_access:  read_only
        .address_space:  global
        .offset:         200
        .size:           8
        .value_kind:     global_buffer
      - .actual_access:  read_only
        .address_space:  global
        .offset:         208
        .size:           8
        .value_kind:     global_buffer
      - .actual_access:  read_only
        .address_space:  global
        .offset:         216
        .size:           8
        .value_kind:     global_buffer
      - .actual_access:  read_only
        .address_space:  global
        .offset:         224
        .size:           8
        .value_kind:     global_buffer
      - .actual_access:  write_only
        .address_space:  global
        .offset:         232
        .size:           8
        .value_kind:     global_buffer
      - .actual_access:  write_only
        .address_space:  global
        .offset:         240
        .size:           8
        .value_kind:     global_buffer
      - .actual_access:  read_only
        .address_space:  global
        .offset:         248
        .size:           8
        .value_kind:     global_buffer
      - .actual_access:  write_only
        .address_space:  global
        .offset:         256
        .size:           8
        .value_kind:     global_buffer
    .group_segment_fixed_size: 37412
    .kernarg_segment_align: 8
    .kernarg_segment_size: 264
    .language:       OpenCL C
    .language_version:
      - 2
      - 0
    .max_flat_workgroup_size: 256
    .name:           _Z6k_prep8PrepArgsPKfS1_S1_S1_PDv8_DF16_PfS1_S4_
    .private_segment_fixed_size: 0
    .sgpr_count:     36
    .sgpr_spill_count: 0
    .symbol:         _Z6k_prep8PrepArgsPKfS1_S1_S1_PDv8_DF16_PfS1_S4_.kd
    .uniform_work_group_size: 1
    .uses_dynamic_stack: false
    .vgpr_count:     80
    .vgpr_spill_count: 0
    .wavefront_size: 64
  - .agpr_count:     0
    .args:
      - .actual_access:  read_only
        .address_space:  global
        .offset:         0
        .size:           8
        .value_kind:     global_buffer
      - .actual_access:  read_only
        .address_space:  global
        .offset:         8
        .size:           8
        .value_kind:     global_buffer
      - .actual_access:  read_only
        .address_space:  global
        .offset:         16
        .size:           8
        .value_kind:     global_buffer
      - .actual_access:  read_only
        .address_space:  global
        .offset:         24
        .size:           8
        .value_kind:     global_buffer
      - .actual_access:  read_only
        .address_space:  global
        .offset:         32
        .size:           8
        .value_kind:     global_buffer
      - .actual_access:  read_only
        .address_space:  global
        .offset:         40
        .size:           8
        .value_kind:     global_buffer
      - .actual_access:  write_only
        .address_space:  global
        .offset:         48
        .size:           8
        .value_kind:     global_buffer
      - .actual_access:  write_only
        .address_space:  global
        .offset:         56
        .size:           8
        .value_kind:     global_buffer
      - .actual_access:  write_only
        .address_space:  global
        .offset:         64
        .size:           8
        .value_kind:     global_buffer
      - .actual_access:  write_only
        .address_space:  global
        .offset:         72
        .size:           8
        .value_kind:     global_buffer
      - .offset:         80
        .size:           4
        .value_kind:     hidden_block_count_x
      - .offset:         84
        .size:           4
        .value_kind:     hidden_block_count_y
      - .offset:         88
        .size:           4
        .value_kind:     hidden_block_count_z
      - .offset:         92
        .size:           2
        .value_kind:     hidden_group_size_x
      - .offset:         94
        .size:           2
        .value_kind:     hidden_group_size_y
      - .offset:         96
        .size:           2
        .value_kind:     hidden_group_size_z
      - .offset:         98
        .size:           2
        .value_kind:     hidden_remainder_x
      - .offset:         100
        .size:           2
        .value_kind:     hidden_remainder_y
      - .offset:         102
        .size:           2
        .value_kind:     hidden_remainder_z
      - .offset:         120
        .size:           8
        .value_kind:     hidden_global_offset_x
      - .offset:         128
        .size:           8
        .value_kind:     hidden_global_offset_y
      - .offset:         136
        .size:           8
        .value_kind:     hidden_global_offset_z
      - .offset:         144
        .size:           2
        .value_kind:     hidden_grid_dims
    .group_segment_fixed_size: 72208
    .kernarg_segment_align: 8
    .kernarg_segment_size: 336
    .language:       OpenCL C
    .language_version:
      - 2
      - 0
    .max_flat_workgroup_size: 256
    .name:           _Z8k_projvqPKfPKDv8_DF16_S0_S3_S0_S0_PfS4_PiS4_
    .private_segment_fixed_size: 0
    .sgpr_count:     49
    .sgpr_spill_count: 0
    .symbol:         _Z8k_projvqPKfPKDv8_DF16_S0_S3_S0_S0_PfS4_PiS4_.kd
    .uniform_work_group_size: 1
    .uses_dynamic_stack: false
    .vgpr_count:     174
    .vgpr_spill_count: 0
    .wavefront_size: 64
  - .agpr_count:     0
    .args:
      - .actual_access:  read_only
        .address_space:  global
        .offset:         0
        .size:           8
        .value_kind:     global_buffer
      - .actual_access:  read_only
        .address_space:  global
        .offset:         8
        .size:           8
        .value_kind:     global_buffer
      - .actual_access:  write_only
        .address_space:  global
        .offset:         16
        .size:           8
        .value_kind:     global_buffer
      - .actual_access:  write_only
        .address_space:  global
        .offset:         24
        .size:           8
        .value_kind:     global_buffer
      - .offset:         32
        .size:           4
        .value_kind:     hidden_block_count_x
      - .offset:         36
        .size:           4
        .value_kind:     hidden_block_count_y
      - .offset:         40
        .size:           4
        .value_kind:     hidden_block_count_z
      - .offset:         44
        .size:           2
        .value_kind:     hidden_group_size_x
      - .offset:         46
        .size:           2
        .value_kind:     hidden_group_size_y
      - .offset:         48
        .size:           2
        .value_kind:     hidden_group_size_z
      - .offset:         50
        .size:           2
        .value_kind:     hidden_remainder_x
      - .offset:         52
        .size:           2
        .value_kind:     hidden_remainder_y
      - .offset:         54
        .size:           2
        .value_kind:     hidden_remainder_z
      - .offset:         72
        .size:           8
        .value_kind:     hidden_global_offset_x
      - .offset:         80
        .size:           8
        .value_kind:     hidden_global_offset_y
      - .offset:         88
        .size:           8
        .value_kind:     hidden_global_offset_z
      - .offset:         96
        .size:           2
        .value_kind:     hidden_grid_dims
    .group_segment_fixed_size: 16
    .kernarg_segment_align: 8
    .kernarg_segment_size: 288
    .language:       OpenCL C
    .language_version:
      - 2
      - 0
    .max_flat_workgroup_size: 256
    .name:           _Z10k_upsamplePKfS0_PfS1_
    .private_segment_fixed_size: 0
    .sgpr_count:     22
    .sgpr_spill_count: 0
    .symbol:         _Z10k_upsamplePKfS0_PfS1_.kd
    .uniform_work_group_size: 1
    .uses_dynamic_stack: false
    .vgpr_count:     44
    .vgpr_spill_count: 0
    .wavefront_size: 64
  - .agpr_count:     0
    .args:
      - .actual_access:  read_only
        .address_space:  global
        .offset:         0
        .size:           8
        .value_kind:     global_buffer
      - .offset:         8
        .size:           4
        .value_kind:     by_value
      - .actual_access:  read_only
        .address_space:  global
        .offset:         16
        .size:           8
        .value_kind:     global_buffer
      - .offset:         24
        .size:           4
        .value_kind:     by_value
      - .actual_access:  write_only
        .address_space:  global
        .offset:         32
        .size:           8
        .value_kind:     global_buffer
    .group_segment_fixed_size: 16384
    .kernarg_segment_align: 8
    .kernarg_segment_size: 40
    .language:       OpenCL C
    .language_version:
      - 2
      - 0
    .max_flat_workgroup_size: 1024
    .name:           _Z10k_finalizePKfiS0_iPf
    .private_segment_fixed_size: 0
    .sgpr_count:     21
    .sgpr_spill_count: 0
    .symbol:         _Z10k_finalizePKfiS0_iPf.kd
    .uniform_work_group_size: 1
    .uses_dynamic_stack: false
    .vgpr_count:     44
    .vgpr_spill_count: 0
    .wavefront_size: 64
  - .agpr_count:     0
    .args:
      - .actual_access:  read_only
        .address_space:  global
        .offset:         0
        .size:           8
        .value_kind:     global_buffer
      - .actual_access:  read_only
        .address_space:  global
        .offset:         8
        .size:           8
        .value_kind:     global_buffer
      - .actual_access:  read_only
        .address_space:  global
        .offset:         16
        .size:           8
        .value_kind:     global_buffer
      - .actual_access:  write_only
        .address_space:  global
        .offset:         24
        .size:           8
        .value_kind:     global_buffer
      - .offset:         32
        .size:           4
        .value_kind:     by_value
      - .offset:         36
        .size:           4
        .value_kind:     by_value
      - .offset:         40
        .size:           4
        .value_kind:     by_value
      - .offset:         44
        .size:           4
        .value_kind:     by_value
    .group_segment_fixed_size: 46800
    .kernarg_segment_align: 8
    .kernarg_segment_size: 48
    .language:       OpenCL C
    .language_version:
      - 2
      - 0
    .max_flat_workgroup_size: 256
    .name:           _Z11k_conv1_t14I3GeoILi64ELi16ELi3ELi2EEEvPKfPKDv8_DF16_S3_Pfiiii
    .private_segment_fixed_size: 0
    .sgpr_count:     66
    .sgpr_spill_count: 0
    .symbol:         _Z11k_conv1_t14I3GeoILi64ELi16ELi3ELi2EEEvPKfPKDv8_DF16_S3_Pfiiii.kd
    .uniform_work_group_size: 1
    .uses_dynamic_stack: false
    .vgpr_count:     198
    .vgpr_spill_count: 0
    .wavefront_size: 64
  - .agpr_count:     0
    .args:
      - .actual_access:  read_only
        .address_space:  global
        .offset:         0
        .size:           8
        .value_kind:     global_buffer
      - .actual_access:  read_only
        .address_space:  global
        .offset:         8
        .size:           8
        .value_kind:     global_buffer
      - .actual_access:  read_only
        .address_space:  global
        .offset:         16
        .size:           8
        .value_kind:     global_buffer
      - .actual_access:  read_only
        .address_space:  global
        .offset:         24
        .size:           8
        .value_kind:     global_buffer
      - .actual_access:  read_only
        .address_space:  global
        .offset:         32
        .size:           8
        .value_kind:     global_buffer
      - .actual_access:  read_only
        .address_space:  global
        .offset:         40
        .size:           8
        .value_kind:     global_buffer
      - .actual_access:  read_only
        .address_space:  global
        .offset:         48
        .size:           8
        .value_kind:     global_buffer
      - .actual_access:  read_only
        .address_space:  global
        .offset:         56
        .size:           8
        .value_kind:     global_buffer
      - .actual_access:  write_only
        .address_space:  global
        .offset:         64
        .size:           8
        .value_kind:     global_buffer
      - .actual_access:  write_only
        .address_space:  global
        .offset:         72
        .size:           8
        .value_kind:     global_buffer
      - .actual_access:  write_only
        .address_space:  global
        .offset:         80
        .size:           8
        .value_kind:     global_buffer
      - .actual_access:  write_only
        .address_space:  global
        .offset:         88
        .size:           8
        .value_kind:     global_buffer
      - .offset:         96
        .size:           4
        .value_kind:     by_value
      - .offset:         100
        .size:           4
        .value_kind:     by_value
      - .offset:         104
        .size:           4
        .value_kind:     hidden_block_count_x
      - .offset:         108
        .size:           4
        .value_kind:     hidden_block_count_y
      - .offset:         112
        .size:           4
        .value_kind:     hidden_block_count_z
      - .offset:         116
        .size:           2
        .value_kind:     hidden_group_size_x
      - .offset:         118
        .size:           2
        .value_kind:     hidden_group_size_y
      - .offset:         120
        .size:           2
        .value_kind:     hidden_group_size_z
      - .offset:         122
        .size:           2
        .value_kind:     hidden_remainder_x
      - .offset:         124
        .size:           2
        .value_kind:     hidden_remainder_y
      - .offset:         126
        .size:           2
        .value_kind:     hidden_remainder_z
      - .offset:         144
        .size:           8
        .value_kind:     hidden_global_offset_x
      - .offset:         152
        .size:           8
        .value_kind:     hidden_global_offset_y
      - .offset:         160
        .size:           8
        .value_kind:     hidden_global_offset_z
      - .offset:         168
        .size:           2
        .value_kind:     hidden_grid_dims
    .group_segment_fixed_size: 139264
    .kernarg_segment_align: 8
    .kernarg_segment_size: 360
    .language:       OpenCL C
    .language_version:
      - 2
      - 0
    .max_flat_workgroup_size: 512
    .name:           _Z7k_c2pvqI3GeoILi128ELi16ELi3ELi2EEEvPKfPKDv8_DF16_S3_S6_S3_S6_S3_S3_PfS7_PiS7_ii
    .private_segment_fixed_size: 0
    .sgpr_count:     64
    .sgpr_spill_count: 0
    .symbol:         _Z7k_c2pvqI3GeoILi128ELi16ELi3ELi2EEEvPKfPKDv8_DF16_S3_S6_S3_S6_S3_S3_PfS7_PiS7_ii.kd
    .uniform_work_group_size: 1
    .uses_dynamic_stack: false
    .vgpr_count:     256
    .vgpr_spill_count: 0
    .wavefront_size: 64
  - .agpr_count:     0
    .args:
      - .actual_access:  read_only
        .address_space:  global
        .offset:         0
        .size:           8
        .value_kind:     global_buffer
      - .actual_access:  read_only
        .address_space:  global
        .offset:         8
        .size:           8
        .value_kind:     global_buffer
      - .actual_access:  read_only
        .address_space:  global
        .offset:         16
        .size:           8
        .value_kind:     global_buffer
      - .actual_access:  read_only
        .address_space:  global
        .offset:         24
        .size:           8
        .value_kind:     global_buffer
      - .actual_access:  read_only
        .address_space:  global
        .offset:         32
        .size:           8
        .value_kind:     global_buffer
      - .actual_access:  read_only
        .address_space:  global
        .offset:         40
        .size:           8
        .value_kind:     global_buffer
      - .actual_access:  write_only
        .address_space:  global
        .offset:         48
        .size:           8
        .value_kind:     global_buffer
      - .offset:         56
        .size:           4
        .value_kind:     by_value
      - .offset:         60
        .size:           4
        .value_kind:     by_value
      - .offset:         64
        .size:           4
        .value_kind:     by_value
      - .offset:         68
        .size:           4
        .value_kind:     by_value
    .group_segment_fixed_size: 67584
    .kernarg_segment_align: 8
    .kernarg_segment_size: 72
    .language:       OpenCL C
    .language_version:
      - 2
      - 0
    .max_flat_workgroup_size: 256
    .name:           _Z12k_recfin_t14I3GeoILi128ELi32ELi3ELi1EEEvPKfPKiPKDv8_DF16_S3_S8_S3_Pfiiii
    .private_segment_fixed_size: 0
    .sgpr_count:     49
    .sgpr_spill_count: 0
    .symbol:         _Z12k_recfin_t14I3GeoILi128ELi32ELi3ELi1EEEvPKfPKiPKDv8_DF16_S3_S8_S3_Pfiiii.kd
    .uniform_work_group_size: 1
    .uses_dynamic_stack: false
    .vgpr_count:     194
    .vgpr_spill_count: 0
    .wavefront_size: 64
